# P7 drain: per-slot progress words prefetched during the P6 epilogue instead of a cold load at the head of the drain
# baseline (speedup 1.0000x reference)
; #define LAS __attribute__((address_space(3)))
;     __device__ void operator()(int r, int n, float v) const { if (r < NMETA) proj[(size_t)(M + r) * DINP + n] = f2bf(v); }
;     __device__ __forceinline__ void operator()(const f32x4 (&acc)[2][2][4][2], const Unit& u, int wr, int wc, int fr, int fq, const LAS float* bl) const {
;         const int row0 = u.pm * BM + wr * 64 + fr, col0 = u.pn * BM + wc * 32 + 4 * fq;
; #pragma unroll
;         for (int ai = 0; ai < 2; ++ai) {
;             f32x4 res[4][2][2];
; #pragma unroll
;             for (int m = 0; m < 4; ++m) { const size_t off = (size_t)(row0 + ai * HALF + m * 16) * ldc + col0;
; #pragma unroll
;                 for (int bj = 0; bj < 2; ++bj)
; #pragma unroll
;                     for (int n = 0; n < 2; ++n) res[m][bj][n] = __builtin_nontemporal_load((const f32x4*)(base + off + bj * HALF + n * 16)); }
; __device__ __forceinline__ void drain_balanced(const Ctx& c, const unsigned* ctl, const float* w_gu, const float* w_d, unsigned char* Wgu, unsigned char* Wd) {
;     ...
;     int n0 = (int)ctl[CW_PROG + 2 * c.tid], n1 = (int)ctl[CW_PROG + 2 * c.tid + 1];
.LBB0_1111:
	s_load_dwordx2 s[98:99], s[94:95], 0xa8
	v_lshlrev_b32_e32 v253, 3, v0
	v_add_u32_e32 v253, 0x2000, v253
	s_waitcnt lgkmcnt(0)
	global_load_dwordx2 v[254:255], v253, s[98:99]
	s_waitcnt lgkmcnt(0)
	v_lshl_add_u32 v184, s75, 8, v213
	v_lshl_or_b32 v130, s54, 8, v214
	v_ashrrev_i32_e32 v185, 31, v184
	v_ashrrev_i32_e32 v131, 31, v130
	v_lshlrev_b64 v[134:135], 13, v[184:185]
	v_or_b32_e32 v152, 16, v184
	v_or_b32_e32 v168, 32, v184
	v_or_b32_e32 v184, 48, v184
	v_lshlrev_b64 v[130:131], 2, v[130:131]
	v_ashrrev_i32_e32 v153, 31, v152
	v_ashrrev_i32_e32 v169, 31, v168
	v_ashrrev_i32_e32 v185, 31, v184
	v_lshl_add_u64 v[132:133], s[12:13], 0, v[130:131]
	v_lshlrev_b64 v[192:193], 13, v[152:153]
	v_lshlrev_b64 v[224:225], 13, v[168:169]
	v_lshlrev_b64 v[226:227], 13, v[184:185]
	v_lshl_add_u64 v[148:149], v[132:133], 0, v[134:135]
	v_lshl_add_u64 v[164:165], v[132:133], 0, v[192:193]
	v_lshl_add_u64 v[180:181], v[132:133], 0, v[224:225]
	v_lshl_add_u64 v[220:221], v[132:133], 0, v[226:227]
	global_load_dwordx4 v[136:139], v[148:149], off nt
	global_load_dwordx4 v[140:143], v[148:149], off offset:64 nt
	global_load_dwordx4 v[144:147], v[148:149], off offset:512 nt
	s_nop 0
	global_load_dwordx4 v[148:151], v[148:149], off offset:576 nt
	s_nop 0
	global_load_dwordx4 v[152:155], v[164:165], off nt
	global_load_dwordx4 v[156:159], v[164:165], off offset:64 nt
	global_load_dwordx4 v[160:163], v[164:165], off offset:512 nt
	s_nop 0
	global_load_dwordx4 v[164:167], v[164:165], off offset:576 nt
	s_nop 0
	global_load_dwordx4 v[168:171], v[180:181], off nt
	global_load_dwordx4 v[172:175], v[180:181], off offset:64 nt
	global_load_dwordx4 v[176:179], v[180:181], off offset:512 nt
	s_nop 0
	global_load_dwordx4 v[180:183], v[180:181], off offset:576 nt
	s_nop 0
	global_load_dwordx4 v[184:187], v[220:221], off nt
	global_load_dwordx4 v[188:191], v[220:221], off offset:64 nt
	global_load_dwordx4 v[206:209], v[220:221], off offset:512 nt
	s_nop 0
	global_load_dwordx4 v[220:223], v[220:221], off offset:576 nt
	v_lshl_add_u64 v[228:229], s[28:29], 0, v[134:135]
	v_lshl_add_u64 v[226:227], s[28:29], 0, v[226:227]
	v_lshl_add_u64 v[228:229], v[228:229], 0, v[130:131]
	v_lshl_add_u64 v[192:193], s[28:29], 0, v[192:193]
	v_lshl_add_u64 v[224:225], s[28:29], 0, v[224:225]
	v_lshl_add_u64 v[226:227], v[226:227], 0, v[130:131]
	v_lshl_add_u64 v[192:193], v[192:193], 0, v[130:131]
	v_lshl_add_u64 v[224:225], v[224:225], 0, v[130:131]
	s_andn2_b64 vcc, exec, s[4:5]
	s_mov_b64 s[4:5], -1
	s_waitcnt vmcnt(0)
;     __device__ __forceinline__ void operator()(const f32x4 (&acc)[2][2][4][2], const Unit& u, int wr, int wc, int fr, int fq, const LAS float* bl) const {
;     ...
;         for (int ai = 0; ai < 2; ++ai) {
;             f32x4 res[4][2][2];
; #pragma unroll
;             for (int m = 0; m < 4; ++m) { const size_t off = (size_t)(row0 + ai * HALF + m * 16) * ldc + col0;
; #pragma unroll
;                 for (int bj = 0; bj < 2; ++bj)
; #pragma unroll
;                     for (int n = 0; n < 2; ++n) res[m][bj][n] = __builtin_nontemporal_load((const f32x4*)(base + off + bj * HALF + n * 16)); }
; #pragma unroll
;             for (int m = 0; m < 4; ++m) { const size_t off = (size_t)(row0 + ai * HALF + m * 16) * ldc + col0;
; #pragma unroll
;                 for (int bj = 0; bj < 2; ++bj)
; #pragma unroll
;                     for (int n = 0; n < 2; ++n) *(f32x4*)(out + off + bj * HALF + n * 16) = res[m][bj][n] + acc[ai][bj][m][n]; }
;         }
	v_pk_add_f32 v[128:129], v[128:129], v[138:139]
	v_pk_add_f32 v[126:127], v[126:127], v[136:137]
	v_pk_add_f32 v[122:123], v[122:123], v[140:141]
	v_pk_add_f32 v[110:111], v[110:111], v[156:157]
	v_pk_add_f32 v[94:95], v[94:95], v[172:173]
	v_pk_add_f32 v[78:79], v[78:79], v[180:181]
	v_pk_add_f32 v[72:73], v[72:73], v[208:209]
	v_pk_add_f32 v[70:71], v[70:71], v[206:207]
	v_pk_add_f32 v[68:69], v[68:69], v[222:223]
	v_pk_add_f32 v[66:67], v[66:67], v[220:221]
	v_lshl_add_u64 v[136:137], v[134:135], 0, s[42:43]
	v_lshl_add_u64 v[138:139], v[134:135], 0, s[44:45]
	v_lshl_add_u64 v[140:141], v[134:135], 0, s[46:47]
	v_lshl_add_u64 v[134:135], v[134:135], 0, s[48:49]
	v_pk_add_f32 v[124:125], v[124:125], v[142:143]
	v_pk_add_f32 v[116:117], v[116:117], v[146:147]
	v_pk_add_f32 v[114:115], v[114:115], v[144:145]
	v_pk_add_f32 v[108:109], v[108:109], v[150:151]
	v_pk_add_f32 v[106:107], v[106:107], v[148:149]
	v_pk_add_f32 v[120:121], v[120:121], v[154:155]
	v_pk_add_f32 v[118:119], v[118:119], v[152:153]
	v_pk_add_f32 v[112:113], v[112:113], v[158:159]
	v_pk_add_f32 v[100:101], v[100:101], v[162:163]
	v_pk_add_f32 v[98:99], v[98:99], v[160:161]
	v_pk_add_f32 v[92:93], v[92:93], v[166:167]
	v_pk_add_f32 v[90:91], v[90:91], v[164:165]
	v_pk_add_f32 v[104:105], v[104:105], v[170:171]
	v_pk_add_f32 v[102:103], v[102:103], v[168:169]
	v_pk_add_f32 v[96:97], v[96:97], v[174:175]
	v_pk_add_f32 v[84:85], v[84:85], v[178:179]
	v_pk_add_f32 v[82:83], v[82:83], v[176:177]
	v_pk_add_f32 v[80:81], v[80:81], v[182:183]
	v_pk_add_f32 v[88:89], v[88:89], v[186:187]
	v_pk_add_f32 v[86:87], v[86:87], v[184:185]
	v_pk_add_f32 v[76:77], v[76:77], v[190:191]
	v_pk_add_f32 v[74:75], v[74:75], v[188:189]
	global_store_dwordx4 v[228:229], v[126:129], off
	global_store_dwordx4 v[228:229], v[122:125], off offset:64
	global_store_dwordx4 v[228:229], v[114:117], off offset:512
	global_store_dwordx4 v[228:229], v[106:109], off offset:576
	global_store_dwordx4 v[192:193], v[118:121], off
	global_store_dwordx4 v[192:193], v[110:113], off offset:64
	global_store_dwordx4 v[192:193], v[98:101], off offset:512
	global_store_dwordx4 v[192:193], v[90:93], off offset:576
	global_store_dwordx4 v[224:225], v[102:105], off
	global_store_dwordx4 v[224:225], v[94:97], off offset:64
	global_store_dwordx4 v[224:225], v[82:85], off offset:512
	global_store_dwordx4 v[224:225], v[78:81], off offset:576
	global_store_dwordx4 v[226:227], v[86:89], off
	global_store_dwordx4 v[226:227], v[74:77], off offset:64
	global_store_dwordx4 v[226:227], v[70:73], off offset:512
	global_store_dwordx4 v[226:227], v[66:69], off offset:576
	v_lshl_add_u64 v[78:79], v[132:133], 0, v[136:137]
	v_lshl_add_u64 v[94:95], v[132:133], 0, v[138:139]
	v_lshl_add_u64 v[110:111], v[132:133], 0, v[140:141]
	v_lshl_add_u64 v[126:127], v[132:133], 0, v[134:135]
	global_load_dwordx4 v[66:69], v[78:79], off nt
	global_load_dwordx4 v[70:73], v[78:79], off offset:64 nt
	global_load_dwordx4 v[74:77], v[78:79], off offset:512 nt
	s_nop 0
	global_load_dwordx4 v[78:81], v[78:79], off offset:576 nt
	s_nop 0
	global_load_dwordx4 v[82:85], v[94:95], off nt
	global_load_dwordx4 v[86:89], v[94:95], off offset:64 nt
	global_load_dwordx4 v[90:93], v[94:95], off offset:512 nt
	s_nop 0
	global_load_dwordx4 v[94:97], v[94:95], off offset:576 nt
	s_nop 0
	global_load_dwordx4 v[98:101], v[110:111], off nt
	global_load_dwordx4 v[102:105], v[110:111], off offset:64 nt
	global_load_dwordx4 v[106:109], v[110:111], off offset:512 nt
	s_nop 0
	global_load_dwordx4 v[110:113], v[110:111], off offset:576 nt
	s_nop 0
	global_load_dwordx4 v[114:117], v[126:127], off nt
	global_load_dwordx4 v[118:121], v[126:127], off offset:64 nt
	global_load_dwordx4 v[122:125], v[126:127], off offset:512 nt
	s_nop 0
	global_load_dwordx4 v[126:129], v[126:127], off offset:576 nt
	v_lshl_add_u64 v[132:133], s[28:29], 0, v[136:137]
	v_lshl_add_u64 v[136:137], s[28:29], 0, v[138:139]
	v_lshl_add_u64 v[138:139], s[28:29], 0, v[140:141]
	v_lshl_add_u64 v[134:135], s[28:29], 0, v[134:135]
	v_lshl_add_u64 v[132:133], v[132:133], 0, v[130:131]
	v_lshl_add_u64 v[136:137], v[136:137], 0, v[130:131]
	v_lshl_add_u64 v[138:139], v[138:139], 0, v[130:131]
	v_lshl_add_u64 v[130:131], v[134:135], 0, v[130:131]
	s_waitcnt vmcnt(15)
	v_pk_add_f32 v[56:57], v[56:57], v[68:69]
	v_pk_add_f32 v[54:55], v[54:55], v[66:67]
	s_waitcnt vmcnt(14)
	v_pk_add_f32 v[52:53], v[52:53], v[72:73]
	v_pk_add_f32 v[50:51], v[50:51], v[70:71]
	s_waitcnt vmcnt(13)
	v_pk_add_f32 v[44:45], v[44:45], v[76:77]
	v_pk_add_f32 v[42:43], v[42:43], v[74:75]
	s_waitcnt vmcnt(0)
	v_pk_add_f32 v[4:5], v[4:5], v[128:129]
	v_pk_add_f32 v[2:3], v[2:3], v[126:127]
	v_pk_add_f32 v[36:37], v[36:37], v[80:81]
	v_pk_add_f32 v[34:35], v[34:35], v[78:79]
	v_pk_add_f32 v[48:49], v[48:49], v[84:85]
	v_pk_add_f32 v[46:47], v[46:47], v[82:83]
	v_pk_add_f32 v[40:41], v[40:41], v[88:89]
	v_pk_add_f32 v[38:39], v[38:39], v[86:87]
	v_pk_add_f32 v[28:29], v[28:29], v[92:93]
	v_pk_add_f32 v[26:27], v[26:27], v[90:91]
	v_pk_add_f32 v[12:13], v[12:13], v[96:97]
	v_pk_add_f32 v[10:11], v[10:11], v[94:95]
	v_pk_add_f32 v[32:33], v[32:33], v[100:101]
	v_pk_add_f32 v[30:31], v[30:31], v[98:99]
	v_pk_add_f32 v[20:21], v[20:21], v[104:105]
	v_pk_add_f32 v[18:19], v[18:19], v[102:103]
	v_pk_add_f32 v[64:65], v[64:65], v[108:109]
	v_pk_add_f32 v[62:63], v[62:63], v[106:107]
	v_pk_add_f32 v[60:61], v[60:61], v[112:113]
	v_pk_add_f32 v[58:59], v[58:59], v[110:111]
	v_pk_add_f32 v[16:17], v[16:17], v[116:117]
	v_pk_add_f32 v[14:15], v[14:15], v[114:115]
	v_pk_add_f32 v[8:9], v[8:9], v[120:121]
	v_pk_add_f32 v[6:7], v[6:7], v[118:119]
	v_pk_add_f32 v[24:25], v[24:25], v[124:125]
	v_pk_add_f32 v[22:23], v[22:23], v[122:123]
	global_store_dwordx4 v[132:133], v[54:57], off
	global_store_dwordx4 v[132:133], v[50:53], off offset:64
	global_store_dwordx4 v[132:133], v[42:45], off offset:512
	global_store_dwordx4 v[132:133], v[34:37], off offset:576
	global_store_dwordx4 v[136:137], v[46:49], off
	global_store_dwordx4 v[136:137], v[38:41], off offset:64
	global_store_dwordx4 v[136:137], v[26:29], off offset:512
	global_store_dwordx4 v[136:137], v[10:13], off offset:576
	global_store_dwordx4 v[138:139], v[30:33], off
	global_store_dwordx4 v[138:139], v[18:21], off offset:64
	global_store_dwordx4 v[138:139], v[62:65], off offset:512
	global_store_dwordx4 v[138:139], v[58:61], off offset:576
	global_store_dwordx4 v[130:131], v[14:17], off
	global_store_dwordx4 v[130:131], v[6:9], off offset:64
	global_store_dwordx4 v[130:131], v[22:25], off offset:512
	global_store_dwordx4 v[130:131], v[2:5], off offset:576
	s_cbranch_vccnz .LBB0_1090
	s_andn2_b64 vcc, exec, s[16:17]
	s_cbranch_vccnz .LBB0_1089
	s_barrier
	s_branch .LBB0_1089

; #define LAS __attribute__((address_space(3)))
; __device__ __forceinline__ void drain_balanced(const Ctx& c, const unsigned* ctl, const float* w_gu, const float* w_d, unsigned char* Wgu, unsigned char* Wd) {
;     LAS int* pre = (LAS int*)(c.lds + DR_OFF); LAS int* prog = pre + 1025; LAS int* wt = prog + 1024;
;     __syncthreads();
;     int n0 = (int)ctl[CW_PROG + 2 * c.tid], n1 = (int)ctl[CW_PROG + 2 * c.tid + 1];
;     const int N0 = (CONV_TOTAL - 2 * c.tid + CONV_SLOTS - 1) / CONV_SLOTS, N1 = (CONV_TOTAL - (2 * c.tid + 1) + CONV_SLOTS - 1) / CONV_SLOTS;
;     const int l0 = N0 > n0 ? N0 - n0 : 0, l1 = N1 > n1 ? N1 - n1 : 0;
;     int incl = l0 + l1;
; #pragma unroll
;     for (int o = 1; o < 64; o <<= 1) { const int v = __shfl_up(incl, o); if (c.lane >= o) incl += v; }
;     if (c.lane == 63) wt[c.wave] = incl;
;     prog[2 * c.tid] = n0; prog[2 * c.tid + 1] = n1;
; __device__ __forceinline__ void phase7() { const Ctx c = make_ctx(); PHASE_PTRS;
;     const bool drain_first = ((c.wg >> 3) & 1) != 0;
;     const unsigned* const ctl7 = (const unsigned*)(ws + WS_CTL);
;     if (drain_first) drain_balanced(c, ctl7, INP(15), INP(17), (unsigned char*)Wgu, (unsigned char*)Wd);
.LBB0_1169:
	v_readlane_b32 s0, v252, 0
	s_cmp_lt_i32 s0, 8
	s_cselect_b64 s[6:7], -1, 0
	s_and_b64 s[28:29], s[6:7], s[4:5]
	s_andn2_b64 vcc, exec, s[28:29]
	v_readlane_b32 s1, v252, 1
	s_cbranch_vccnz .LBB0_1363
	v_mov_b32_e32 v216, v0
	s_mov_b64 s[34:35], s[94:95]
	s_load_dwordx2 s[36:37], s[34:35], 0xa8
	v_readfirstlane_b32 s44, v216
	s_ashr_i32 s56, s44, 6
	s_lshl_b32 s4, s2, 3
	s_add_i32 s57, s56, s4
	s_lshl_b32 s30, s3, 3
	s_waitcnt lgkmcnt(0)
	s_add_u32 s52, s36, 0x1e00000
	s_addc_u32 s53, s37, 0
	s_add_u32 s54, s36, 0x21e00000
	s_addc_u32 s55, s37, 0
	s_bitcmp0_b32 s2, 3
	v_and_b32_e32 v1, 63, v216
	s_cselect_b64 s[38:39], -1, 0
	s_and_b64 vcc, exec, s[38:39]
	v_lshlrev_b32_e32 v162, 1, v216
	v_cmp_ne_u32_e64 s[16:17], 0, v1
	v_cmp_lt_u32_e64 s[14:15], 1, v1
	v_cmp_lt_u32_e64 s[12:13], 3, v1
	v_cmp_lt_u32_e64 s[10:11], 7, v1
	v_cmp_lt_u32_e64 s[8:9], 15, v1
	v_cmp_lt_u32_e64 s[6:7], 31, v1
	v_cmp_eq_u32_e64 s[4:5], 63, v1
	s_cbranch_vccnz .LBB0_1222
	v_ashrrev_i32_e32 v163, 31, v162
	s_waitcnt vmcnt(0)
	v_lshl_add_u64 v[2:3], v[162:163], 2, s[36:37]
	v_add_co_u32_e32 v2, vcc, 0x2000, v2
	s_nop 1
	v_addc_co_u32_e32 v3, vcc, 0, v3, vcc
	s_barrier
	v_readlane_b32 s98, v252, 0
	s_cmp_gt_i32 s98, 6
	s_cbranch_scc1 .Lpf7a_ld
	v_mov_b32_e32 v2, v254
	v_mov_b32_e32 v3, v255
	s_branch .Lpf7a_done
.Lpf7a_ld:
	global_load_dwordx2 v[2:3], v[2:3], off
.Lpf7a_done:
	v_sub_u32_e32 v4, 0x183ff, v162
	v_sub_u32_e32 v5, 0x183fe, v162
	v_mbcnt_lo_u32_b32 v6, -1, 0
	v_ashrrev_i32_e32 v7, 31, v4
	v_ashrrev_i32_e32 v8, 31, v5
	v_mbcnt_hi_u32_b32 v6, -1, v6
	v_lshrrev_b32_e32 v7, 22, v7
	v_lshrrev_b32_e32 v8, 22, v8
	v_and_b32_e32 v9, 64, v6
	v_add_u32_e32 v10, -1, v6
	v_add_u32_e32 v4, v4, v7
	v_add_u32_e32 v5, v5, v8
	v_cmp_lt_i32_e32 vcc, v10, v9
	v_ashrrev_i32_e32 v4, 10, v4
	v_ashrrev_i32_e32 v5, 10, v5
	v_cndmask_b32_e32 v7, v10, v6, vcc
	v_lshlrev_b32_e32 v7, 2, v7
	s_waitcnt vmcnt(0)
	v_sub_u32_e32 v8, v4, v2
	v_cmp_gt_i32_e32 vcc, v4, v2
	v_sub_u32_e32 v10, v5, v3
	s_nop 0
	v_cndmask_b32_e32 v4, 0, v8, vcc
	v_cmp_gt_i32_e32 vcc, v5, v3
	v_add_u32_e32 v8, -2, v6
	s_nop 0
	v_cndmask_b32_e32 v5, 0, v10, vcc
	v_add_u32_e32 v5, v5, v4
	ds_bpermute_b32 v7, v7, v5
	v_cmp_lt_i32_e32 vcc, v8, v9
	v_add_u32_e32 v10, -4, v6
	s_waitcnt lgkmcnt(0)
	v_cndmask_b32_e64 v7, 0, v7, s[16:17]
	v_cndmask_b32_e32 v8, v8, v6, vcc
	v_lshlrev_b32_e32 v8, 2, v8
	v_add_u32_e32 v7, v7, v5
	ds_bpermute_b32 v8, v8, v7
	v_cmp_lt_i32_e32 vcc, v10, v9
	s_waitcnt lgkmcnt(0)
	v_cndmask_b32_e64 v8, 0, v8, s[14:15]
	v_cndmask_b32_e32 v10, v10, v6, vcc
	v_lshlrev_b32_e32 v10, 2, v10
	v_add_u32_e32 v7, v8, v7
	ds_bpermute_b32 v8, v10, v7
	v_add_u32_e32 v10, -8, v6
	v_cmp_lt_i32_e32 vcc, v10, v9
	s_waitcnt lgkmcnt(0)
	v_cndmask_b32_e64 v8, 0, v8, s[12:13]
	v_cndmask_b32_e32 v10, v10, v6, vcc
	v_lshlrev_b32_e32 v10, 2, v10
	v_add_u32_e32 v7, v8, v7
	ds_bpermute_b32 v8, v10, v7
	v_add_u32_e32 v10, -16, v6
	v_cmp_lt_i32_e32 vcc, v10, v9
	s_waitcnt lgkmcnt(0)
	v_cndmask_b32_e64 v8, 0, v8, s[10:11]
	v_cndmask_b32_e32 v10, v10, v6, vcc
	v_lshlrev_b32_e32 v10, 2, v10
	v_add_u32_e32 v7, v8, v7
	ds_bpermute_b32 v8, v10, v7
	v_subrev_u32_e32 v10, 32, v6
	v_cmp_lt_i32_e32 vcc, v10, v9
	s_waitcnt lgkmcnt(0)
	v_cndmask_b32_e64 v8, 0, v8, s[8:9]
	v_cndmask_b32_e32 v6, v10, v6, vcc
	v_add_u32_e32 v7, v8, v7
	v_lshlrev_b32_e32 v6, 2, v6
	ds_bpermute_b32 v6, v6, v7
	s_waitcnt lgkmcnt(0)
	v_cndmask_b32_e64 v6, 0, v6, s[6:7]
	v_add_u32_e32 v6, v6, v7
	s_and_saveexec_b64 s[6:7], s[4:5]
	s_lshl_b32 s4, s56, 2
	s_add_i32 s4, s4, 0
	s_add_i32 s4, s4, 0x23004
	v_mov_b32_e32 v7, s4
	ds_write_b32 v7, v6
	s_or_b64 exec, exec, s[6:7]
	v_lshl_add_u32 v7, v216, 3, 0
	v_add_u32_e32 v8, 0x22004, v7
	s_add_i32 s8, 0, 0x23004
	s_load_dwordx2 s[4:5], s[34:35], 0x78
	s_load_dwordx2 s[6:7], s[34:35], 0x88
	ds_write2_b32 v8, v2, v3 offset1:1
	v_mov_b32_e32 v2, s8
	s_waitcnt lgkmcnt(0)
	s_barrier
; __device__ __forceinline__ void drain_balanced(const Ctx& c, const unsigned* ctl, const float* w_gu, const float* w_d, unsigned char* Wgu, unsigned char* Wd) {
;     ...
;     __syncthreads();
;     int base = 0, total = 0;
; #pragma unroll
;     for (int w = 0; w < NWAVES; ++w) { const int t = wt[w]; base += (w < c.wave) ? t : 0; total += t; }
;     const int excl = base + incl - (l0 + l1);
;     pre[2 * c.tid] = excl; pre[2 * c.tid + 1] = excl + l0;
;     if (c.tid == 0) pre[1024] = total;
;     __syncthreads();
;     const int lo = __builtin_amdgcn_readfirstlane((int)((long long)c.gw * total / c.NGW)), hi = __builtin_amdgcn_readfirstlane((int)((long long)(c.gw + 1) * total / c.NGW));
	ds_read2_b32 v[2:3], v2 offset1:1
	s_cmp_gt_i32 s56, 0
	v_cmp_eq_u32_e32 vcc, 0, v216
	s_waitcnt lgkmcnt(0)
	v_readfirstlane_b32 s8, v2
	v_readfirstlane_b32 s9, v3
	s_cselect_b32 s11, s8, 0
	s_cmp_gt_i32 s56, 1
	s_cselect_b32 s12, s9, 0
	s_add_i32 s10, 0, 0x2300c
	v_mov_b32_e32 v2, s10
	ds_read2_b32 v[2:3], v2 offset1:1
	s_add_i32 s8, s9, s8
	s_cmp_gt_i32 s56, 2
	s_waitcnt lgkmcnt(0)
	v_readfirstlane_b32 s9, v2
	s_cselect_b32 s13, s9, 0
	s_add_i32 s8, s8, s9
	v_readfirstlane_b32 s10, v3
	s_cmp_gt_i32 s56, 3
	s_cselect_b32 s9, s10, 0
	s_add_i32 s14, 0, 0x23014
	v_mov_b32_e32 v2, s14
	ds_read2_b32 v[2:3], v2 offset1:1
	s_add_i32 s8, s8, s10
	s_cmp_gt_i32 s56, 4
	s_waitcnt lgkmcnt(0)
	v_readfirstlane_b32 s10, v2
	s_cselect_b32 s15, s10, 0
	s_add_i32 s8, s8, s10
	v_readfirstlane_b32 s14, v3
	s_cmp_gt_i32 s56, 5
	s_cselect_b32 s17, s14, 0
	s_add_i32 s10, 0, 0x2301c
	v_mov_b32_e32 v2, s10
	ds_read2_b32 v[2:3], v2 offset1:1
	s_add_i32 s8, s8, s14
	s_cmp_gt_i32 s56, 6
	s_mov_b32 s10, 0
	s_waitcnt lgkmcnt(0)
	v_readfirstlane_b32 s14, v2
	s_cselect_b32 s18, s14, 0
	s_add_i32 s8, s8, s14
	v_readfirstlane_b32 s16, v3
	s_cmp_gt_i32 s56, 7
	s_cselect_b32 s14, s16, 0
	s_add_i32 s16, s8, s16
	s_add_i32 s8, s14, s18
	s_add_i32 s8, s8, s17
	s_add_i32 s8, s8, s15
	s_add_i32 s8, s8, s9
	s_add_i32 s8, s8, s13
	s_add_i32 s8, s8, s12
	v_sub_u32_e32 v2, v6, v5
	s_add_i32 s8, s8, s11
	v_add_u32_e32 v2, s8, v2
	v_add_u32_e32 v5, 0x21000, v7
	v_add_u32_e32 v3, v2, v4
	ds_write_b64 v5, v[2:3]
	s_and_saveexec_b64 s[8:9], vcc
	s_add_i32 s11, 0, 0x22000
	v_mov_b32_e32 v2, s11
	v_mov_b32_e32 v3, s16
	ds_write_b32 v2, v3
	s_or_b64 exec, exec, s[8:9]
	s_mul_hi_i32 s9, s16, s57
	s_mul_i32 s8, s16, s57
	s_ashr_i32 s31, s30, 31
	s_or_b64 s[12:13], s[8:9], s[30:31]
	s_mov_b32 s11, s13
	s_cmp_lg_u64 s[10:11], 0
	s_waitcnt lgkmcnt(0)
	s_barrier
	s_cbranch_scc0 .LBB0_1187
	s_ashr_i32 s12, s31, 31
	s_add_u32 s10, s30, s12
	s_mov_b32 s13, s12
	s_addc_u32 s11, s31, s12
	s_xor_b64 s[14:15], s[10:11], s[12:13]
	v_cvt_f32_u32_e32 v2, s14
	v_cvt_f32_u32_e32 v3, s15
	s_sub_u32 s17, 0, s14
	s_subb_u32 s20, 0, s15
	v_fmamk_f32 v2, v3, 0x4f800000, v2
	v_rcp_f32_e32 v2, v2
	s_nop 0
	v_mul_f32_e32 v2, 0x5f7ffffc, v2
	v_mul_f32_e32 v3, 0x2f800000, v2
	v_trunc_f32_e32 v3, v3
	v_fmamk_f32 v2, v3, 0xcf800000, v2
	v_cvt_u32_f32_e32 v3, v3
	v_cvt_u32_f32_e32 v2, v2
	v_readfirstlane_b32 s21, v3
	v_readfirstlane_b32 s18, v2
	s_mul_i32 s19, s17, s21
	s_mul_hi_u32 s25, s17, s18
	s_mul_i32 s24, s20, s18
	s_add_i32 s19, s25, s19
	s_add_i32 s19, s19, s24
	s_mul_i32 s26, s17, s18
	s_mul_i32 s25, s18, s19
	s_mul_hi_u32 s27, s18, s26
	s_mul_hi_u32 s24, s18, s19
	s_add_u32 s25, s27, s25
	s_addc_u32 s24, 0, s24
	s_mul_hi_u32 s40, s21, s26
	s_mul_i32 s26, s21, s26
	s_add_u32 s25, s25, s26
	s_mul_hi_u32 s27, s21, s19
	s_addc_u32 s24, s24, s40
	s_addc_u32 s25, s27, 0
	s_mul_i32 s19, s21, s19
	s_add_u32 s19, s24, s19
	s_addc_u32 s24, 0, s25
	s_add_u32 s25, s18, s19
	s_cselect_b64 s[18:19], -1, 0
	s_cmp_lg_u64 s[18:19], 0
	s_addc_u32 s21, s21, s24
	s_mul_i32 s18, s17, s21
	s_mul_hi_u32 s19, s17, s25
	s_add_i32 s18, s19, s18
	s_mul_i32 s20, s20, s25
	s_add_i32 s18, s18, s20
	s_mul_i32 s17, s17, s25
	s_mul_hi_u32 s20, s21, s17
	s_mul_i32 s24, s21, s17
	s_mul_i32 s27, s25, s18
	s_mul_hi_u32 s17, s25, s17
	s_mul_hi_u32 s26, s25, s18
	s_add_u32 s17, s17, s27
	s_addc_u32 s26, 0, s26
	s_add_u32 s17, s17, s24
	s_mul_hi_u32 s19, s21, s18
	s_addc_u32 s17, s26, s20
	s_addc_u32 s19, s19, 0
	s_mul_i32 s18, s21, s18
	s_add_u32 s17, s17, s18
	s_addc_u32 s20, 0, s19
	s_add_u32 s17, s25, s17
	s_cselect_b64 s[18:19], -1, 0
	s_cmp_lg_u64 s[18:19], 0
	s_addc_u32 s24, s21, s20
	s_ashr_i32 s18, s9, 31
	s_add_u32 s20, s8, s18
	s_mov_b32 s19, s18
	s_addc_u32 s21, s9, s18
	s_xor_b64 s[20:21], s[20:21], s[18:19]
	s_mul_i32 s25, s20, s24
	s_mul_hi_u32 s26, s20, s17
	s_mul_hi_u32 s9, s20, s24
	s_add_u32 s25, s26, s25
	s_addc_u32 s9, 0, s9
	s_mul_hi_u32 s27, s21, s17
	s_mul_i32 s17, s21, s17
	s_add_u32 s17, s25, s17
	s_mul_hi_u32 s26, s21, s24
	s_addc_u32 s9, s9, s27
	s_addc_u32 s17, s26, 0
	s_mul_i32 s24, s21, s24
	s_add_u32 s9, s9, s24
	s_addc_u32 s17, 0, s17
	s_mul_i32 s24, s14, s17
	s_mul_hi_u32 s25, s14, s9
	s_add_i32 s24, s25, s24
	s_mul_i32 s25, s15, s9
	s_add_i32 s40, s24, s25
	s_sub_i32 s26, s21, s40
	s_mul_i32 s24, s14, s9
	s_sub_u32 s20, s20, s24
	s_cselect_b64 s[24:25], -1, 0
	s_cmp_lg_u64 s[24:25], 0
	s_subb_u32 s41, s26, s15
	s_sub_u32 s42, s20, s14
	s_cselect_b64 s[26:27], -1, 0
	s_cmp_lg_u64 s[26:27], 0
	s_subb_u32 s26, s41, 0
	s_cmp_ge_u32 s26, s15
	s_cselect_b32 s27, -1, 0
	s_cmp_ge_u32 s42, s14
	s_cselect_b32 s41, -1, 0
	s_cmp_eq_u32 s26, s15
	s_cselect_b32 s26, s41, s27
	s_add_u32 s27, s9, 1
	s_addc_u32 s41, s17, 0
	s_add_u32 s42, s9, 2
	s_addc_u32 s43, s17, 0
	s_cmp_lg_u32 s26, 0
	s_cselect_b32 s26, s42, s27
	s_cselect_b32 s27, s43, s41
	s_cmp_lg_u64 s[24:25], 0
	s_subb_u32 s21, s21, s40
	s_cmp_ge_u32 s21, s15
	s_cselect_b32 s24, -1, 0
	s_cmp_ge_u32 s20, s14
	s_cselect_b32 s14, -1, 0
	s_cmp_eq_u32 s21, s15
	s_cselect_b32 s14, s14, s24
	s_cmp_lg_u32 s14, 0
	s_cselect_b32 s15, s27, s17
	s_cselect_b32 s14, s26, s9
	s_xor_b64 s[12:13], s[18:19], s[12:13]
	s_xor_b64 s[14:15], s[14:15], s[12:13]
	s_sub_u32 s12, s14, s12
	s_subb_u32 s13, s15, s13
	v_cvt_f32_u32_e32 v4, s30
	v_mov_b64_e32 v[2:3], s[12:13]
	s_cbranch_execnz .LBB0_1178

; #define LAS __attribute__((address_space(3)))
; __device__ __forceinline__ void drain_balanced(const Ctx& c, const unsigned* ctl, const float* w_gu, const float* w_d, unsigned char* Wgu, unsigned char* Wd) {
;     LAS int* pre = (LAS int*)(c.lds + DR_OFF); LAS int* prog = pre + 1025; LAS int* wt = prog + 1024;
;     __syncthreads();
;     int n0 = (int)ctl[CW_PROG + 2 * c.tid], n1 = (int)ctl[CW_PROG + 2 * c.tid + 1];
; __device__ __forceinline__ void phase7() { const Ctx c = make_ctx(); PHASE_PTRS;
;     ...
;     if (!drain_first) drain_balanced(c, ctl7, INP(15), INP(17), (unsigned char*)Wgu, (unsigned char*)Wd);
.LBB0_1311:
	s_and_b64 vcc, exec, s[38:39]
	s_cbranch_vccz .LBB0_1363
	v_ashrrev_i32_e32 v163, 31, v162
	s_waitcnt vmcnt(0)
	v_lshl_add_u64 v[2:3], v[162:163], 2, s[36:37]
	v_add_co_u32_e32 v2, vcc, 0x2000, v2
	s_nop 1
	v_addc_co_u32_e32 v3, vcc, 0, v3, vcc
	s_barrier
	v_readlane_b32 s98, v252, 0
	s_cmp_gt_i32 s98, 6
	s_cbranch_scc1 .Lpf7b_ld
	v_mov_b32_e32 v2, v254
	v_mov_b32_e32 v3, v255
	s_branch .Lpf7b_done

; __device__ __forceinline__ void drain_balanced(const Ctx& c, const unsigned* ctl, const float* w_gu, const float* w_d, unsigned char* Wgu, unsigned char* Wd) {
;     ...
;     int n0 = (int)ctl[CW_PROG + 2 * c.tid], n1 = (int)ctl[CW_PROG + 2 * c.tid + 1];
;     const int N0 = (CONV_TOTAL - 2 * c.tid + CONV_SLOTS - 1) / CONV_SLOTS, N1 = (CONV_TOTAL - (2 * c.tid + 1) + CONV_SLOTS - 1) / CONV_SLOTS;
;     const int l0 = N0 > n0 ? N0 - n0 : 0, l1 = N1 > n1 ? N1 - n1 : 0;
;     int incl = l0 + l1;
; #pragma unroll
;     for (int o = 1; o < 64; o <<= 1) { const int v = __shfl_up(incl, o); if (c.lane >= o) incl += v; }
;     if (c.lane == 63) wt[c.wave] = incl;
;     prog[2 * c.tid] = n0; prog[2 * c.tid + 1] = n1;
;     __syncthreads();
;     int base = 0, total = 0;
; #pragma unroll
;     for (int w = 0; w < NWAVES; ++w) { const int t = wt[w]; base += (w < c.wave) ? t : 0; total += t; }
;     const int excl = base + incl - (l0 + l1);
;     pre[2 * c.tid] = excl; pre[2 * c.tid + 1] = excl + l0;
;     if (c.tid == 0) pre[1024] = total;
.Lpf7b_done:
	v_sub_u32_e32 v4, 0x183ff, v162
	v_sub_u32_e32 v5, 0x183fe, v162
	v_mbcnt_lo_u32_b32 v6, -1, 0
	v_ashrrev_i32_e32 v7, 31, v4
	v_ashrrev_i32_e32 v8, 31, v5
	v_mbcnt_hi_u32_b32 v6, -1, v6
	v_lshrrev_b32_e32 v7, 22, v7
	v_lshrrev_b32_e32 v8, 22, v8
	v_and_b32_e32 v9, 64, v6
	v_add_u32_e32 v10, -1, v6
	v_add_u32_e32 v4, v4, v7
	v_add_u32_e32 v5, v5, v8
	v_cmp_lt_i32_e32 vcc, v10, v9
	v_ashrrev_i32_e32 v4, 10, v4
	v_ashrrev_i32_e32 v5, 10, v5
	v_cndmask_b32_e32 v7, v10, v6, vcc
	v_lshlrev_b32_e32 v7, 2, v7
	v_add_u32_e32 v11, -2, v6
	v_add_u32_e32 v12, -4, v6
	v_add_u32_e32 v13, -8, v6
	v_add_u32_e32 v14, -16, v6
	v_subrev_u32_e32 v15, 32, v6
	s_waitcnt vmcnt(0)
	v_sub_u32_e32 v8, v4, v2
	v_cmp_gt_i32_e32 vcc, v4, v2
	v_sub_u32_e32 v10, v5, v3
	s_nop 0
	v_cndmask_b32_e32 v4, 0, v8, vcc
	v_cmp_gt_i32_e32 vcc, v5, v3
	s_nop 1
	v_cndmask_b32_e32 v5, 0, v10, vcc
	v_add_u32_e32 v5, v5, v4
	ds_bpermute_b32 v7, v7, v5
	v_cmp_lt_i32_e32 vcc, v11, v9
	s_nop 1
	v_cndmask_b32_e32 v8, v11, v6, vcc
	v_cmp_ne_u32_e32 vcc, 0, v1
	v_lshlrev_b32_e32 v8, 2, v8
	s_waitcnt lgkmcnt(0)
	v_cndmask_b32_e32 v7, 0, v7, vcc
	v_add_u32_e32 v7, v7, v5
	ds_bpermute_b32 v8, v8, v7
	v_cmp_lt_i32_e32 vcc, v12, v9
	s_nop 1
	v_cndmask_b32_e32 v10, v12, v6, vcc
	v_cmp_lt_u32_e32 vcc, 1, v1
	v_lshlrev_b32_e32 v10, 2, v10
	s_waitcnt lgkmcnt(0)
	v_cndmask_b32_e32 v8, 0, v8, vcc
	v_add_u32_e32 v7, v8, v7
	ds_bpermute_b32 v8, v10, v7
	v_cmp_lt_i32_e32 vcc, v13, v9
	s_nop 1
	v_cndmask_b32_e32 v10, v13, v6, vcc
	v_cmp_lt_u32_e32 vcc, 3, v1
	v_lshlrev_b32_e32 v10, 2, v10
	s_waitcnt lgkmcnt(0)
	v_cndmask_b32_e32 v8, 0, v8, vcc
	v_add_u32_e32 v7, v8, v7
	ds_bpermute_b32 v8, v10, v7
	v_cmp_lt_i32_e32 vcc, v14, v9
	s_nop 1
	v_cndmask_b32_e32 v10, v14, v6, vcc
	v_cmp_lt_u32_e32 vcc, 7, v1
	v_lshlrev_b32_e32 v10, 2, v10
	s_waitcnt lgkmcnt(0)
	v_cndmask_b32_e32 v8, 0, v8, vcc
	v_add_u32_e32 v7, v8, v7
	ds_bpermute_b32 v8, v10, v7
	v_cmp_lt_i32_e32 vcc, v15, v9
	s_nop 1
	v_cndmask_b32_e32 v6, v15, v6, vcc
	v_cmp_lt_u32_e32 vcc, 15, v1
	v_lshlrev_b32_e32 v6, 2, v6
	s_waitcnt lgkmcnt(0)
	v_cndmask_b32_e32 v8, 0, v8, vcc
	v_add_u32_e32 v7, v8, v7
	ds_bpermute_b32 v6, v6, v7
	v_cmp_lt_u32_e32 vcc, 31, v1
	s_waitcnt lgkmcnt(0)
	s_nop 0
	v_cndmask_b32_e32 v6, 0, v6, vcc
	v_add_u32_e32 v6, v6, v7
	v_cmp_eq_u32_e32 vcc, 63, v1
	s_and_saveexec_b64 s[4:5], vcc
	s_lshl_b32 s6, s56, 2
	s_add_i32 s6, s6, 0
	s_add_i32 s6, s6, 0x23004
	v_mov_b32_e32 v7, s6
	ds_write_b32 v7, v6
	s_or_b64 exec, exec, s[4:5]
	v_lshl_add_u32 v7, v216, 3, 0
	v_add_u32_e32 v8, 0x22004, v7
	s_add_i32 s8, 0, 0x23004
	s_load_dwordx2 s[4:5], s[34:35], 0x78
	s_load_dwordx2 s[6:7], s[34:35], 0x88
	ds_write2_b32 v8, v2, v3 offset1:1
	v_mov_b32_e32 v2, s8
	s_waitcnt lgkmcnt(0)
	s_barrier
	ds_read2_b32 v[2:3], v2 offset1:1
	s_cmp_gt_i32 s56, 0
	v_cmp_eq_u32_e32 vcc, 0, v216
	s_waitcnt lgkmcnt(0)
	v_readfirstlane_b32 s8, v2
	v_readfirstlane_b32 s9, v3
	s_cselect_b32 s10, s8, 0
	s_cmp_gt_i32 s56, 1
	s_cselect_b32 s11, s9, 0
	s_add_i32 s12, 0, 0x2300c
	v_mov_b32_e32 v2, s12
	ds_read2_b32 v[2:3], v2 offset1:1
	s_add_i32 s8, s9, s8
	s_cmp_gt_i32 s56, 2
	s_waitcnt lgkmcnt(0)
	v_readfirstlane_b32 s9, v2
	s_cselect_b32 s13, s9, 0
	s_add_i32 s8, s8, s9
	v_readfirstlane_b32 s12, v3
	s_cmp_gt_i32 s56, 3
	s_cselect_b32 s9, s12, 0
	s_add_i32 s14, 0, 0x23014
	v_mov_b32_e32 v2, s14
	ds_read2_b32 v[2:3], v2 offset1:1
	s_add_i32 s8, s8, s12
	s_cmp_gt_i32 s56, 4
	s_waitcnt lgkmcnt(0)
	v_readfirstlane_b32 s12, v2
	s_cselect_b32 s15, s12, 0
	s_add_i32 s8, s8, s12
	v_readfirstlane_b32 s14, v3
	s_cmp_gt_i32 s56, 5
	s_cselect_b32 s12, s14, 0
	s_add_i32 s16, 0, 0x2301c
	v_mov_b32_e32 v2, s16
	ds_read2_b32 v[2:3], v2 offset1:1
	s_add_i32 s8, s8, s14
	s_cmp_gt_i32 s56, 6
	s_waitcnt lgkmcnt(0)
	v_readfirstlane_b32 s14, v2
	s_cselect_b32 s17, s14, 0
	s_add_i32 s8, s8, s14
	v_readfirstlane_b32 s16, v3
	s_cmp_gt_i32 s56, 7
	s_cselect_b32 s14, s16, 0
	s_add_i32 s16, s8, s16
	s_add_i32 s8, s14, s17
	s_add_i32 s8, s8, s12
	s_add_i32 s8, s8, s15
	s_add_i32 s8, s8, s9
	s_add_i32 s8, s8, s13
	s_add_i32 s8, s8, s11
	v_sub_u32_e32 v2, v6, v5
	s_add_i32 s8, s8, s10
	v_add_u32_e32 v2, s8, v2
	v_add_u32_e32 v5, 0x21000, v7
	v_add_u32_e32 v3, v2, v4
	ds_write_b64 v5, v[2:3]
	s_and_saveexec_b64 s[8:9], vcc
	s_add_i32 s10, 0, 0x22000
	v_mov_b32_e32 v2, s10
	v_mov_b32_e32 v3, s16
	ds_write_b32 v2, v3
	s_or_b64 exec, exec, s[8:9]
	s_mul_hi_i32 s9, s16, s57
	s_mul_i32 s8, s16, s57
	s_ashr_i32 s31, s30, 31
	s_or_b64 s[10:11], s[8:9], s[30:31]
	s_mov_b32 s10, 0
	s_cmp_lg_u64 s[10:11], 0
	s_waitcnt lgkmcnt(0)
	s_barrier
; __device__ __forceinline__ void drain_balanced(const Ctx& c, const unsigned* ctl, const float* w_gu, const float* w_d, unsigned char* Wgu, unsigned char* Wd) {
;     ...
;     const int lo = __builtin_amdgcn_readfirstlane((int)((long long)c.gw * total / c.NGW)), hi = __builtin_amdgcn_readfirstlane((int)((long long)(c.gw + 1) * total / c.NGW));
	s_cbranch_scc0 .LBB0_1328
	s_ashr_i32 s12, s31, 31
	s_add_u32 s10, s30, s12
	s_mov_b32 s13, s12
	s_addc_u32 s11, s31, s12
	s_xor_b64 s[14:15], s[10:11], s[12:13]
	v_cvt_f32_u32_e32 v2, s14
	v_cvt_f32_u32_e32 v3, s15
	s_sub_u32 s17, 0, s14
	s_subb_u32 s20, 0, s15
	v_fmamk_f32 v2, v3, 0x4f800000, v2
	v_rcp_f32_e32 v2, v2
	s_nop 0
	v_mul_f32_e32 v2, 0x5f7ffffc, v2
	v_mul_f32_e32 v3, 0x2f800000, v2
	v_trunc_f32_e32 v3, v3
	v_fmamk_f32 v2, v3, 0xcf800000, v2
	v_cvt_u32_f32_e32 v3, v3
	v_cvt_u32_f32_e32 v2, v2
	v_readfirstlane_b32 s21, v3
	v_readfirstlane_b32 s18, v2
	s_mul_i32 s19, s17, s21
	s_mul_hi_u32 s25, s17, s18
	s_mul_i32 s24, s20, s18
	s_add_i32 s19, s25, s19
	s_add_i32 s19, s19, s24
	s_mul_i32 s26, s17, s18
	s_mul_i32 s25, s18, s19
	s_mul_hi_u32 s27, s18, s26
	s_mul_hi_u32 s24, s18, s19
	s_add_u32 s25, s27, s25
	s_addc_u32 s24, 0, s24
	s_mul_hi_u32 s34, s21, s26
	s_mul_i32 s26, s21, s26
	s_add_u32 s25, s25, s26
	s_mul_hi_u32 s27, s21, s19
	s_addc_u32 s24, s24, s34
	s_addc_u32 s25, s27, 0
	s_mul_i32 s19, s21, s19
	s_add_u32 s19, s24, s19
	s_addc_u32 s24, 0, s25
	s_add_u32 s25, s18, s19
	s_cselect_b64 s[18:19], -1, 0
	s_cmp_lg_u64 s[18:19], 0
	s_addc_u32 s21, s21, s24
	s_mul_i32 s18, s17, s21
	s_mul_hi_u32 s19, s17, s25
	s_add_i32 s18, s19, s18
	s_mul_i32 s20, s20, s25
	s_add_i32 s18, s18, s20
	s_mul_i32 s17, s17, s25
	s_mul_hi_u32 s20, s21, s17
	s_mul_i32 s24, s21, s17
	s_mul_i32 s27, s25, s18
	s_mul_hi_u32 s17, s25, s17
	s_mul_hi_u32 s26, s25, s18
	s_add_u32 s17, s17, s27
	s_addc_u32 s26, 0, s26
	s_add_u32 s17, s17, s24
	s_mul_hi_u32 s19, s21, s18
	s_addc_u32 s17, s26, s20
	s_addc_u32 s19, s19, 0
	s_mul_i32 s18, s21, s18
	s_add_u32 s17, s17, s18
	s_addc_u32 s20, 0, s19
	s_add_u32 s17, s25, s17
	s_cselect_b64 s[18:19], -1, 0
	s_cmp_lg_u64 s[18:19], 0
	s_addc_u32 s24, s21, s20
	s_ashr_i32 s18, s9, 31
	s_add_u32 s20, s8, s18
	s_mov_b32 s19, s18
	s_addc_u32 s21, s9, s18
	s_xor_b64 s[20:21], s[20:21], s[18:19]
	s_mul_i32 s25, s20, s24
	s_mul_hi_u32 s26, s20, s17
	s_mul_hi_u32 s9, s20, s24
	s_add_u32 s25, s26, s25
	s_addc_u32 s9, 0, s9
	s_mul_hi_u32 s27, s21, s17
	s_mul_i32 s17, s21, s17
	s_add_u32 s17, s25, s17
	s_mul_hi_u32 s26, s21, s24
	s_addc_u32 s9, s9, s27
	s_addc_u32 s17, s26, 0
	s_mul_i32 s24, s21, s24
	s_add_u32 s9, s9, s24
	s_addc_u32 s17, 0, s17
	s_mul_i32 s24, s14, s17
	s_mul_hi_u32 s25, s14, s9
	s_add_i32 s24, s25, s24
	s_mul_i32 s25, s15, s9
	s_add_i32 s34, s24, s25
	s_sub_i32 s26, s21, s34
	s_mul_i32 s24, s14, s9
	s_sub_u32 s20, s20, s24
	s_cselect_b64 s[24:25], -1, 0
	s_cmp_lg_u64 s[24:25], 0
	s_subb_u32 s35, s26, s15
	s_sub_u32 s36, s20, s14
	s_cselect_b64 s[26:27], -1, 0
	s_cmp_lg_u64 s[26:27], 0
	s_subb_u32 s26, s35, 0
	s_cmp_ge_u32 s26, s15
	s_cselect_b32 s27, -1, 0
	s_cmp_ge_u32 s36, s14
	s_cselect_b32 s35, -1, 0
	s_cmp_eq_u32 s26, s15
	s_cselect_b32 s26, s35, s27
	s_add_u32 s27, s9, 1
	s_addc_u32 s35, s17, 0
	s_add_u32 s36, s9, 2
	s_addc_u32 s37, s17, 0
	s_cmp_lg_u32 s26, 0
	s_cselect_b32 s26, s36, s27
	s_cselect_b32 s27, s37, s35
	s_cmp_lg_u64 s[24:25], 0
	s_subb_u32 s21, s21, s34
	s_cmp_ge_u32 s21, s15
	s_cselect_b32 s24, -1, 0
	s_cmp_ge_u32 s20, s14
	s_cselect_b32 s14, -1, 0
	s_cmp_eq_u32 s21, s15
	s_cselect_b32 s14, s14, s24
	s_cmp_lg_u32 s14, 0
	s_cselect_b32 s15, s27, s17
	s_cselect_b32 s14, s26, s9
	s_xor_b64 s[12:13], s[18:19], s[12:13]
	s_xor_b64 s[14:15], s[14:15], s[12:13]
	s_sub_u32 s12, s14, s12
	s_subb_u32 s13, s15, s13
	v_cvt_f32_u32_e32 v4, s30
	v_mov_b64_e32 v[2:3], s[12:13]
	s_cbranch_execnz .LBB0_1319

; __global__ void __launch_bounds__(NWAVES * 64, 2) mk_fwd(Args a) {
	.amdhsa_kernel _Z6mk_fwd4Args
		.amdhsa_group_segment_fixed_size 0
		.amdhsa_private_segment_fixed_size 0
		.amdhsa_kernarg_size 440
		.amdhsa_user_sgpr_count 2
		.amdhsa_user_sgpr_dispatch_ptr 0
		.amdhsa_user_sgpr_queue_ptr 0
		.amdhsa_user_sgpr_kernarg_segment_ptr 1
		.amdhsa_user_sgpr_dispatch_id 0
		.amdhsa_user_sgpr_kernarg_preload_length 0
		.amdhsa_user_sgpr_kernarg_preload_offset 0
		.amdhsa_user_sgpr_private_segment_size 0
		.amdhsa_uses_dynamic_stack 0
		.amdhsa_enable_private_segment 0
		.amdhsa_system_sgpr_workgroup_id_x 1
		.amdhsa_system_sgpr_workgroup_id_y 0
		.amdhsa_system_sgpr_workgroup_id_z 0
		.amdhsa_system_sgpr_workgroup_info 0
		.amdhsa_system_vgpr_workitem_id 0
		.amdhsa_next_free_vgpr 256
		.amdhsa_next_free_sgpr 100
		.amdhsa_accum_offset 256
		.amdhsa_reserve_vcc 1
		.amdhsa_float_round_mode_32 0
		.amdhsa_float_round_mode_16_64 0
		.amdhsa_float_denorm_mode_32 3
		.amdhsa_float_denorm_mode_16_64 3
		.amdhsa_dx10_clamp 1
		.amdhsa_ieee_mode 1
		.amdhsa_fp16_overflow 0
		.amdhsa_tg_split 0
		.amdhsa_exception_fp_ieee_invalid_op 0
		.amdhsa_exception_fp_denorm_src 0
		.amdhsa_exception_fp_ieee_div_zero 0
		.amdhsa_exception_fp_ieee_overflow 0
		.amdhsa_exception_fp_ieee_underflow 0
		.amdhsa_exception_fp_ieee_inexact 0
		.amdhsa_exception_int_div_zero 0
	.end_amdhsa_kernel

; __global__ void __launch_bounds__(NWAVES * 64, 2) mk_fwd(Args a) {
amdhsa.kernels:
  - .agpr_count:     0
    .args:
      - .offset:         0
        .size:           184
        .value_kind:     by_value
      - .offset:         184
        .size:           4
        .value_kind:     hidden_block_count_x
      - .offset:         188
        .size:           4
        .value_kind:     hidden_block_count_y
      - .offset:         192
        .size:           4
        .value_kind:     hidden_block_count_z
      - .offset:         196
        .size:           2
        .value_kind:     hidden_group_size_x
      - .offset:         198
        .size:           2
        .value_kind:     hidden_group_size_y
      - .offset:         200
        .size:           2
        .value_kind:     hidden_group_size_z
      - .offset:         202
        .size:           2
        .value_kind:     hidden_remainder_x
      - .offset:         204
        .size:           2
        .value_kind:     hidden_remainder_y
      - .offset:         206
        .size:           2
        .value_kind:     hidden_remainder_z
      - .offset:         224
        .size:           8
        .value_kind:     hidden_global_offset_x
      - .offset:         232
        .size:           8
        .value_kind:     hidden_global_offset_y
      - .offset:         240
        .size:           8
        .value_kind:     hidden_global_offset_z
      - .offset:         248
        .size:           2
        .value_kind:     hidden_grid_dims
      - .offset:         304
        .size:           4
        .value_kind:     hidden_dynamic_lds_size
    .group_segment_fixed_size: 0
    .kernarg_segment_align: 8
    .kernarg_segment_size: 440
    .language:       OpenCL C
    .language_version:
      - 2
      - 0
    .max_flat_workgroup_size: 512
    .name:           _Z6mk_fwd4Args
    .private_segment_fixed_size: 0
    .sgpr_count:     106
    .sgpr_spill_count: 21
    .symbol:         _Z6mk_fwd4Args.kd
    .uniform_work_group_size: 1
    .uses_dynamic_stack: false
    .vgpr_count:     256
    .vgpr_spill_count: 0
    .wavefront_size: 64
